# phase 6: hand-scheduled H2 (fp8 rows) pass for the 256-grid case, all 32 row loads in flight, scale/shift read once
# speedup vs baseline: 1.0118x; 1.0011x over previous
; __device__ __forceinline__ void phase_router(const Args& a, unsigned char* lds_g, int tid, int lane, int wave) {
;     ...
;         __syncthreads();
; #pragma unroll
;         for (int r = 0; r < 4; ++r) { const int tl = 4 * kq + r, t = tok0 + tl; const float rstd = RS[slot * 16 + tl];
;             const unsigned long long* xrow = (const unsigned long long*)(X1 + (size_t)t * D) + lane; unsigned* o4 = (unsigned*)((unsigned char*)H2 + (size_t)t * D) + lane;
;             f32x4 yv[8];
; #pragma unroll
;             for (int j = 0; j < 8; ++j) { const int c = 4 * lane + 256 * j;
;                 f32x4 gs, sh; if (shp) { gs = PSH[lane + 64 * j]; sh = PSH[512 + lane + 64 * j]; } else { const f32x4 gg = *(const f32x4*)(g + c), sc = *(const f32x4*)(MOD + b * 12288 + 4 * 2048 + c); gs = gg * (sc + 1.f); sh = *(const f32x4*)(MOD + b * 12288 + 3 * 2048 + c); }
;                 const unsigned long long xw = xrow[64 * j]; const f32x4 xv4 = (f32x4){bflo((unsigned)xw), bfhi((unsigned)xw), bflo((unsigned)(xw >> 32)), bfhi((unsigned)(xw >> 32))};
;                 yv[j] = xv4 * rstd * gs + sh; }
; #pragma unroll
;             for (int j = 0; j < 8; ++j) { int w8 = __builtin_amdgcn_cvt_pk_fp8_f32(yv[j].x, yv[j].y, 0, false); w8 = __builtin_amdgcn_cvt_pk_fp8_f32(yv[j].z, yv[j].w, w8, true); o4[64 * j] = (unsigned)w8; } }
.LBB0_985:
	s_mul_i32 s4, s30, 0x3000
	s_ashr_i32 s5, s4, 31
	s_lshl_b64 s[4:5], s[4:5], 2
	s_add_u32 s4, s2, s4
	s_addc_u32 s5, s3, s5
	v_mov_b32_e32 v0, s40
	s_waitcnt lgkmcnt(0)
	s_barrier
	s_and_b64 vcc, exec, s[18:19]
	s_cbranch_vccnz .Lh2_old
	s_or_b32 s28, s56, s37
	s_lshl_b32 s4, s28, 12
	s_mov_b32 s5, 0
	v_lshl_add_u64 v[210:211], v[66:67], 0, s[4:5]
	global_load_dwordx2 v[114:115], v[210:211], off
	global_load_dwordx2 v[116:117], v[210:211], off offset:512
	global_load_dwordx2 v[118:119], v[210:211], off offset:1024
	global_load_dwordx2 v[120:121], v[210:211], off offset:1536
	global_load_dwordx2 v[122:123], v[210:211], off offset:2048
	global_load_dwordx2 v[124:125], v[210:211], off offset:2560
	global_load_dwordx2 v[126:127], v[210:211], off offset:3072
	global_load_dwordx2 v[128:129], v[210:211], off offset:3584
	s_add_u32 s4, s4, 0x1000
	v_lshl_add_u64 v[210:211], v[66:67], 0, s[4:5]
	global_load_dwordx2 v[130:131], v[210:211], off
	global_load_dwordx2 v[132:133], v[210:211], off offset:512
	global_load_dwordx2 v[134:135], v[210:211], off offset:1024
	global_load_dwordx2 v[136:137], v[210:211], off offset:1536
	global_load_dwordx2 v[138:139], v[210:211], off offset:2048
	global_load_dwordx2 v[140:141], v[210:211], off offset:2560
	global_load_dwordx2 v[142:143], v[210:211], off offset:3072
	global_load_dwordx2 v[144:145], v[210:211], off offset:3584
	s_add_u32 s4, s4, 0x1000
	v_lshl_add_u64 v[210:211], v[66:67], 0, s[4:5]
	global_load_dwordx2 v[146:147], v[210:211], off
	global_load_dwordx2 v[148:149], v[210:211], off offset:512
	global_load_dwordx2 v[150:151], v[210:211], off offset:1024
	global_load_dwordx2 v[152:153], v[210:211], off offset:1536
	global_load_dwordx2 v[154:155], v[210:211], off offset:2048
	global_load_dwordx2 v[156:157], v[210:211], off offset:2560
	global_load_dwordx2 v[158:159], v[210:211], off offset:3072
	global_load_dwordx2 v[160:161], v[210:211], off offset:3584
	s_add_u32 s4, s4, 0x1000
	v_lshl_add_u64 v[210:211], v[66:67], 0, s[4:5]
	global_load_dwordx2 v[162:163], v[210:211], off
	global_load_dwordx2 v[164:165], v[210:211], off offset:512
	global_load_dwordx2 v[166:167], v[210:211], off offset:1024
	global_load_dwordx2 v[168:169], v[210:211], off offset:1536
	global_load_dwordx2 v[170:171], v[210:211], off offset:2048
	global_load_dwordx2 v[172:173], v[210:211], off offset:2560
	global_load_dwordx2 v[194:195], v[210:211], off offset:3072
	global_load_dwordx2 v[196:197], v[210:211], off offset:3584
	v_mov_b32_e32 v212, s40
	ds_read_b32 v202, v212 offset:50176
	ds_read_b32 v204, v212 offset:50180
	ds_read_b32 v206, v212 offset:50184
	ds_read_b32 v208, v212 offset:50188
	ds_read_b128 v[0:3], v183
	ds_read_b128 v[4:7], v183 offset:1024
	ds_read_b128 v[8:11], v183 offset:2048
	ds_read_b128 v[12:15], v183 offset:3072
	ds_read_b128 v[16:19], v183 offset:4096
	ds_read_b128 v[20:23], v183 offset:5120
	ds_read_b128 v[24:27], v183 offset:6144
	ds_read_b128 v[28:31], v183 offset:7168
	ds_read_b128 v[32:35], v183 offset:8192
	ds_read_b128 v[36:39], v183 offset:9216
	ds_read_b128 v[40:43], v183 offset:10240
	ds_read_b128 v[44:47], v183 offset:11264
	ds_read_b128 v[48:51], v183 offset:12288
	ds_read_b128 v[52:55], v183 offset:13312
	ds_read_b128 v[56:59], v183 offset:14336
	ds_read_b128 v[198:201], v183 offset:15360
	s_lshl_b32 s4, s28, 11
	s_waitcnt lgkmcnt(0)
	v_lshl_add_u64 v[210:211], v[68:69], 0, s[4:5]
	s_waitcnt vmcnt(24)
	v_lshlrev_b32_e32 v212, 16, v114
	v_and_b32_e32 v213, 0xffff0000, v114
	v_pk_mul_f32 v[212:213], v[202:203], v[212:213] op_sel_hi:[0,1]
	v_lshlrev_b32_e32 v114, 16, v115
	v_and_b32_e32 v115, 0xffff0000, v115
	v_pk_mul_f32 v[114:115], v[202:203], v[114:115] op_sel_hi:[0,1]
	v_pk_fma_f32 v[212:213], v[0:1], v[212:213], v[32:33]
	v_pk_fma_f32 v[114:115], v[2:3], v[114:115], v[34:35]
	v_cvt_pk_fp8_f32 v214, v212, v213
	v_cvt_pk_fp8_f32 v214, v114, v115 op_sel:[0,0,1]
	global_store_dword v[210:211], v214, off
	v_lshlrev_b32_e32 v212, 16, v116
	v_and_b32_e32 v213, 0xffff0000, v116
	v_pk_mul_f32 v[212:213], v[202:203], v[212:213] op_sel_hi:[0,1]
	v_lshlrev_b32_e32 v116, 16, v117
	v_and_b32_e32 v117, 0xffff0000, v117
	v_pk_mul_f32 v[116:117], v[202:203], v[116:117] op_sel_hi:[0,1]
	v_pk_fma_f32 v[212:213], v[4:5], v[212:213], v[36:37]
	v_pk_fma_f32 v[116:117], v[6:7], v[116:117], v[38:39]
	v_cvt_pk_fp8_f32 v215, v212, v213
	v_cvt_pk_fp8_f32 v215, v116, v117 op_sel:[0,0,1]
	global_store_dword v[210:211], v215, off offset:256
	v_lshlrev_b32_e32 v212, 16, v118
	v_and_b32_e32 v213, 0xffff0000, v118
	v_pk_mul_f32 v[212:213], v[202:203], v[212:213] op_sel_hi:[0,1]
	v_lshlrev_b32_e32 v118, 16, v119
	v_and_b32_e32 v119, 0xffff0000, v119
	v_pk_mul_f32 v[118:119], v[202:203], v[118:119] op_sel_hi:[0,1]
	v_pk_fma_f32 v[212:213], v[8:9], v[212:213], v[40:41]
	v_pk_fma_f32 v[118:119], v[10:11], v[118:119], v[42:43]
	v_cvt_pk_fp8_f32 v214, v212, v213
	v_cvt_pk_fp8_f32 v214, v118, v119 op_sel:[0,0,1]
	global_store_dword v[210:211], v214, off offset:512
	v_lshlrev_b32_e32 v212, 16, v120
	v_and_b32_e32 v213, 0xffff0000, v120
	v_pk_mul_f32 v[212:213], v[202:203], v[212:213] op_sel_hi:[0,1]
	v_lshlrev_b32_e32 v120, 16, v121
	v_and_b32_e32 v121, 0xffff0000, v121
	v_pk_mul_f32 v[120:121], v[202:203], v[120:121] op_sel_hi:[0,1]
	v_pk_fma_f32 v[212:213], v[12:13], v[212:213], v[44:45]
	v_pk_fma_f32 v[120:121], v[14:15], v[120:121], v[46:47]
	v_cvt_pk_fp8_f32 v215, v212, v213
	v_cvt_pk_fp8_f32 v215, v120, v121 op_sel:[0,0,1]
	global_store_dword v[210:211], v215, off offset:768
	v_lshlrev_b32_e32 v212, 16, v122
	v_and_b32_e32 v213, 0xffff0000, v122
	v_pk_mul_f32 v[212:213], v[202:203], v[212:213] op_sel_hi:[0,1]
; __device__ __forceinline__ void phase_router(const Args& a, unsigned char* lds_g, int tid, int lane, int wave) {
;     ...
;         for (int r = 0; r < 4; ++r) { const int tl = 4 * kq + r, t = tok0 + tl; const float rstd = RS[slot * 16 + tl];
;             const unsigned long long* xrow = (const unsigned long long*)(X1 + (size_t)t * D) + lane; unsigned* o4 = (unsigned*)((unsigned char*)H2 + (size_t)t * D) + lane;
;             f32x4 yv[8];
; #pragma unroll
;             for (int j = 0; j < 8; ++j) { const int c = 4 * lane + 256 * j;
;                 f32x4 gs, sh; if (shp) { gs = PSH[lane + 64 * j]; sh = PSH[512 + lane + 64 * j]; } else { const f32x4 gg = *(const f32x4*)(g + c), sc = *(const f32x4*)(MOD + b * 12288 + 4 * 2048 + c); gs = gg * (sc + 1.f); sh = *(const f32x4*)(MOD + b * 12288 + 3 * 2048 + c); }
;                 const unsigned long long xw = xrow[64 * j]; const f32x4 xv4 = (f32x4){bflo((unsigned)xw), bfhi((unsigned)xw), bflo((unsigned)(xw >> 32)), bfhi((unsigned)(xw >> 32))};
;                 yv[j] = xv4 * rstd * gs + sh; }
; #pragma unroll
;             for (int j = 0; j < 8; ++j) { int w8 = __builtin_amdgcn_cvt_pk_fp8_f32(yv[j].x, yv[j].y, 0, false); w8 = __builtin_amdgcn_cvt_pk_fp8_f32(yv[j].z, yv[j].w, w8, true); o4[64 * j] = (unsigned)w8; } }
	v_lshlrev_b32_e32 v122, 16, v123
	v_and_b32_e32 v123, 0xffff0000, v123
	v_pk_mul_f32 v[122:123], v[202:203], v[122:123] op_sel_hi:[0,1]
	v_pk_fma_f32 v[212:213], v[16:17], v[212:213], v[48:49]
	v_pk_fma_f32 v[122:123], v[18:19], v[122:123], v[50:51]
	v_cvt_pk_fp8_f32 v214, v212, v213
	v_cvt_pk_fp8_f32 v214, v122, v123 op_sel:[0,0,1]
	global_store_dword v[210:211], v214, off offset:1024
	v_lshlrev_b32_e32 v212, 16, v124
	v_and_b32_e32 v213, 0xffff0000, v124
	v_pk_mul_f32 v[212:213], v[202:203], v[212:213] op_sel_hi:[0,1]
	v_lshlrev_b32_e32 v124, 16, v125
	v_and_b32_e32 v125, 0xffff0000, v125
	v_pk_mul_f32 v[124:125], v[202:203], v[124:125] op_sel_hi:[0,1]
	v_pk_fma_f32 v[212:213], v[20:21], v[212:213], v[52:53]
	v_pk_fma_f32 v[124:125], v[22:23], v[124:125], v[54:55]
	v_cvt_pk_fp8_f32 v215, v212, v213
	v_cvt_pk_fp8_f32 v215, v124, v125 op_sel:[0,0,1]
	global_store_dword v[210:211], v215, off offset:1280
	v_lshlrev_b32_e32 v212, 16, v126
	v_and_b32_e32 v213, 0xffff0000, v126
	v_pk_mul_f32 v[212:213], v[202:203], v[212:213] op_sel_hi:[0,1]
	v_lshlrev_b32_e32 v126, 16, v127
	v_and_b32_e32 v127, 0xffff0000, v127
	v_pk_mul_f32 v[126:127], v[202:203], v[126:127] op_sel_hi:[0,1]
	v_pk_fma_f32 v[212:213], v[24:25], v[212:213], v[56:57]
	v_pk_fma_f32 v[126:127], v[26:27], v[126:127], v[58:59]
	v_cvt_pk_fp8_f32 v214, v212, v213
	v_cvt_pk_fp8_f32 v214, v126, v127 op_sel:[0,0,1]
	global_store_dword v[210:211], v214, off offset:1536
	v_lshlrev_b32_e32 v212, 16, v128
	v_and_b32_e32 v213, 0xffff0000, v128
	v_pk_mul_f32 v[212:213], v[202:203], v[212:213] op_sel_hi:[0,1]
	v_lshlrev_b32_e32 v128, 16, v129
	v_and_b32_e32 v129, 0xffff0000, v129
	v_pk_mul_f32 v[128:129], v[202:203], v[128:129] op_sel_hi:[0,1]
	v_pk_fma_f32 v[212:213], v[28:29], v[212:213], v[198:199]
	v_pk_fma_f32 v[128:129], v[30:31], v[128:129], v[200:201]
	v_cvt_pk_fp8_f32 v215, v212, v213
	v_cvt_pk_fp8_f32 v215, v128, v129 op_sel:[0,0,1]
	global_store_dword v[210:211], v215, off offset:1792
	s_add_u32 s4, s4, 0x800
	v_lshl_add_u64 v[210:211], v[68:69], 0, s[4:5]
	s_waitcnt vmcnt(24)
	v_lshlrev_b32_e32 v212, 16, v130
	v_and_b32_e32 v213, 0xffff0000, v130
	v_pk_mul_f32 v[212:213], v[204:205], v[212:213] op_sel_hi:[0,1]
	v_lshlrev_b32_e32 v130, 16, v131
	v_and_b32_e32 v131, 0xffff0000, v131
	v_pk_mul_f32 v[130:131], v[204:205], v[130:131] op_sel_hi:[0,1]
	v_pk_fma_f32 v[212:213], v[0:1], v[212:213], v[32:33]
	v_pk_fma_f32 v[130:131], v[2:3], v[130:131], v[34:35]
	v_cvt_pk_fp8_f32 v214, v212, v213
	v_cvt_pk_fp8_f32 v214, v130, v131 op_sel:[0,0,1]
	global_store_dword v[210:211], v214, off
	v_lshlrev_b32_e32 v212, 16, v132
	v_and_b32_e32 v213, 0xffff0000, v132
	v_pk_mul_f32 v[212:213], v[204:205], v[212:213] op_sel_hi:[0,1]
	v_lshlrev_b32_e32 v132, 16, v133
	v_and_b32_e32 v133, 0xffff0000, v133
	v_pk_mul_f32 v[132:133], v[204:205], v[132:133] op_sel_hi:[0,1]
	v_pk_fma_f32 v[212:213], v[4:5], v[212:213], v[36:37]
	v_pk_fma_f32 v[132:133], v[6:7], v[132:133], v[38:39]
	v_cvt_pk_fp8_f32 v215, v212, v213
	v_cvt_pk_fp8_f32 v215, v132, v133 op_sel:[0,0,1]
	global_store_dword v[210:211], v215, off offset:256
	v_lshlrev_b32_e32 v212, 16, v134
	v_and_b32_e32 v213, 0xffff0000, v134
	v_pk_mul_f32 v[212:213], v[204:205], v[212:213] op_sel_hi:[0,1]
	v_lshlrev_b32_e32 v134, 16, v135
	v_and_b32_e32 v135, 0xffff0000, v135
	v_pk_mul_f32 v[134:135], v[204:205], v[134:135] op_sel_hi:[0,1]
	v_pk_fma_f32 v[212:213], v[8:9], v[212:213], v[40:41]
	v_pk_fma_f32 v[134:135], v[10:11], v[134:135], v[42:43]
	v_cvt_pk_fp8_f32 v214, v212, v213
	v_cvt_pk_fp8_f32 v214, v134, v135 op_sel:[0,0,1]
	global_store_dword v[210:211], v214, off offset:512
	v_lshlrev_b32_e32 v212, 16, v136
	v_and_b32_e32 v213, 0xffff0000, v136
	v_pk_mul_f32 v[212:213], v[204:205], v[212:213] op_sel_hi:[0,1]
	v_lshlrev_b32_e32 v136, 16, v137
	v_and_b32_e32 v137, 0xffff0000, v137
	v_pk_mul_f32 v[136:137], v[204:205], v[136:137] op_sel_hi:[0,1]
	v_pk_fma_f32 v[212:213], v[12:13], v[212:213], v[44:45]
	v_pk_fma_f32 v[136:137], v[14:15], v[136:137], v[46:47]
	v_cvt_pk_fp8_f32 v215, v212, v213
	v_cvt_pk_fp8_f32 v215, v136, v137 op_sel:[0,0,1]
	global_store_dword v[210:211], v215, off offset:768
	v_lshlrev_b32_e32 v212, 16, v138
	v_and_b32_e32 v213, 0xffff0000, v138
	v_pk_mul_f32 v[212:213], v[204:205], v[212:213] op_sel_hi:[0,1]
	v_lshlrev_b32_e32 v138, 16, v139
	v_and_b32_e32 v139, 0xffff0000, v139
	v_pk_mul_f32 v[138:139], v[204:205], v[138:139] op_sel_hi:[0,1]
	v_pk_fma_f32 v[212:213], v[16:17], v[212:213], v[48:49]
	v_pk_fma_f32 v[138:139], v[18:19], v[138:139], v[50:51]
	v_cvt_pk_fp8_f32 v214, v212, v213
	v_cvt_pk_fp8_f32 v214, v138, v139 op_sel:[0,0,1]
	global_store_dword v[210:211], v214, off offset:1024
	v_lshlrev_b32_e32 v212, 16, v140
	v_and_b32_e32 v213, 0xffff0000, v140
	v_pk_mul_f32 v[212:213], v[204:205], v[212:213] op_sel_hi:[0,1]
	v_lshlrev_b32_e32 v140, 16, v141
	v_and_b32_e32 v141, 0xffff0000, v141
	v_pk_mul_f32 v[140:141], v[204:205], v[140:141] op_sel_hi:[0,1]
	v_pk_fma_f32 v[212:213], v[20:21], v[212:213], v[52:53]
	v_pk_fma_f32 v[140:141], v[22:23], v[140:141], v[54:55]
	v_cvt_pk_fp8_f32 v215, v212, v213
	v_cvt_pk_fp8_f32 v215, v140, v141 op_sel:[0,0,1]
	global_store_dword v[210:211], v215, off offset:1280
	v_lshlrev_b32_e32 v212, 16, v142
	v_and_b32_e32 v213, 0xffff0000, v142
	v_pk_mul_f32 v[212:213], v[204:205], v[212:213] op_sel_hi:[0,1]
	v_lshlrev_b32_e32 v142, 16, v143
	v_and_b32_e32 v143, 0xffff0000, v143
	v_pk_mul_f32 v[142:143], v[204:205], v[142:143] op_sel_hi:[0,1]
	v_pk_fma_f32 v[212:213], v[24:25], v[212:213], v[56:57]
	v_pk_fma_f32 v[142:143], v[26:27], v[142:143], v[58:59]
	v_cvt_pk_fp8_f32 v214, v212, v213
	v_cvt_pk_fp8_f32 v214, v142, v143 op_sel:[0,0,1]
	global_store_dword v[210:211], v214, off offset:1536
	v_lshlrev_b32_e32 v212, 16, v144
	v_and_b32_e32 v213, 0xffff0000, v144
	v_pk_mul_f32 v[212:213], v[204:205], v[212:213] op_sel_hi:[0,1]
	v_lshlrev_b32_e32 v144, 16, v145
	v_and_b32_e32 v145, 0xffff0000, v145
	v_pk_mul_f32 v[144:145], v[204:205], v[144:145] op_sel_hi:[0,1]
	v_pk_fma_f32 v[212:213], v[28:29], v[212:213], v[198:199]
	v_pk_fma_f32 v[144:145], v[30:31], v[144:145], v[200:201]
	v_cvt_pk_fp8_f32 v215, v212, v213
	v_cvt_pk_fp8_f32 v215, v144, v145 op_sel:[0,0,1]
	global_store_dword v[210:211], v215, off offset:1792
	s_add_u32 s4, s4, 0x800
	v_lshl_add_u64 v[210:211], v[68:69], 0, s[4:5]
	s_waitcnt vmcnt(24)
; __device__ __forceinline__ void phase_router(const Args& a, unsigned char* lds_g, int tid, int lane, int wave) {
;     ...
;         for (int r = 0; r < 4; ++r) { const int tl = 4 * kq + r, t = tok0 + tl; const float rstd = RS[slot * 16 + tl];
;             const unsigned long long* xrow = (const unsigned long long*)(X1 + (size_t)t * D) + lane; unsigned* o4 = (unsigned*)((unsigned char*)H2 + (size_t)t * D) + lane;
;             f32x4 yv[8];
; #pragma unroll
;             for (int j = 0; j < 8; ++j) { const int c = 4 * lane + 256 * j;
;                 f32x4 gs, sh; if (shp) { gs = PSH[lane + 64 * j]; sh = PSH[512 + lane + 64 * j]; } else { const f32x4 gg = *(const f32x4*)(g + c), sc = *(const f32x4*)(MOD + b * 12288 + 4 * 2048 + c); gs = gg * (sc + 1.f); sh = *(const f32x4*)(MOD + b * 12288 + 3 * 2048 + c); }
;                 const unsigned long long xw = xrow[64 * j]; const f32x4 xv4 = (f32x4){bflo((unsigned)xw), bfhi((unsigned)xw), bflo((unsigned)(xw >> 32)), bfhi((unsigned)(xw >> 32))};
;                 yv[j] = xv4 * rstd * gs + sh; }
; #pragma unroll
;             for (int j = 0; j < 8; ++j) { int w8 = __builtin_amdgcn_cvt_pk_fp8_f32(yv[j].x, yv[j].y, 0, false); w8 = __builtin_amdgcn_cvt_pk_fp8_f32(yv[j].z, yv[j].w, w8, true); o4[64 * j] = (unsigned)w8; } }
	v_lshlrev_b32_e32 v212, 16, v146
	v_and_b32_e32 v213, 0xffff0000, v146
	v_pk_mul_f32 v[212:213], v[206:207], v[212:213] op_sel_hi:[0,1]
	v_lshlrev_b32_e32 v146, 16, v147
	v_and_b32_e32 v147, 0xffff0000, v147
	v_pk_mul_f32 v[146:147], v[206:207], v[146:147] op_sel_hi:[0,1]
	v_pk_fma_f32 v[212:213], v[0:1], v[212:213], v[32:33]
	v_pk_fma_f32 v[146:147], v[2:3], v[146:147], v[34:35]
	v_cvt_pk_fp8_f32 v214, v212, v213
	v_cvt_pk_fp8_f32 v214, v146, v147 op_sel:[0,0,1]
	global_store_dword v[210:211], v214, off
	v_lshlrev_b32_e32 v212, 16, v148
	v_and_b32_e32 v213, 0xffff0000, v148
	v_pk_mul_f32 v[212:213], v[206:207], v[212:213] op_sel_hi:[0,1]
	v_lshlrev_b32_e32 v148, 16, v149
	v_and_b32_e32 v149, 0xffff0000, v149
	v_pk_mul_f32 v[148:149], v[206:207], v[148:149] op_sel_hi:[0,1]
	v_pk_fma_f32 v[212:213], v[4:5], v[212:213], v[36:37]
	v_pk_fma_f32 v[148:149], v[6:7], v[148:149], v[38:39]
	v_cvt_pk_fp8_f32 v215, v212, v213
	v_cvt_pk_fp8_f32 v215, v148, v149 op_sel:[0,0,1]
	global_store_dword v[210:211], v215, off offset:256
	v_lshlrev_b32_e32 v212, 16, v150
	v_and_b32_e32 v213, 0xffff0000, v150
	v_pk_mul_f32 v[212:213], v[206:207], v[212:213] op_sel_hi:[0,1]
	v_lshlrev_b32_e32 v150, 16, v151
	v_and_b32_e32 v151, 0xffff0000, v151
	v_pk_mul_f32 v[150:151], v[206:207], v[150:151] op_sel_hi:[0,1]
	v_pk_fma_f32 v[212:213], v[8:9], v[212:213], v[40:41]
	v_pk_fma_f32 v[150:151], v[10:11], v[150:151], v[42:43]
	v_cvt_pk_fp8_f32 v214, v212, v213
	v_cvt_pk_fp8_f32 v214, v150, v151 op_sel:[0,0,1]
	global_store_dword v[210:211], v214, off offset:512
	v_lshlrev_b32_e32 v212, 16, v152
	v_and_b32_e32 v213, 0xffff0000, v152
	v_pk_mul_f32 v[212:213], v[206:207], v[212:213] op_sel_hi:[0,1]
	v_lshlrev_b32_e32 v152, 16, v153
	v_and_b32_e32 v153, 0xffff0000, v153
	v_pk_mul_f32 v[152:153], v[206:207], v[152:153] op_sel_hi:[0,1]
	v_pk_fma_f32 v[212:213], v[12:13], v[212:213], v[44:45]
	v_pk_fma_f32 v[152:153], v[14:15], v[152:153], v[46:47]
	v_cvt_pk_fp8_f32 v215, v212, v213
	v_cvt_pk_fp8_f32 v215, v152, v153 op_sel:[0,0,1]
	global_store_dword v[210:211], v215, off offset:768
	v_lshlrev_b32_e32 v212, 16, v154
	v_and_b32_e32 v213, 0xffff0000, v154
	v_pk_mul_f32 v[212:213], v[206:207], v[212:213] op_sel_hi:[0,1]
	v_lshlrev_b32_e32 v154, 16, v155
	v_and_b32_e32 v155, 0xffff0000, v155
	v_pk_mul_f32 v[154:155], v[206:207], v[154:155] op_sel_hi:[0,1]
	v_pk_fma_f32 v[212:213], v[16:17], v[212:213], v[48:49]
	v_pk_fma_f32 v[154:155], v[18:19], v[154:155], v[50:51]
	v_cvt_pk_fp8_f32 v214, v212, v213
	v_cvt_pk_fp8_f32 v214, v154, v155 op_sel:[0,0,1]
	global_store_dword v[210:211], v214, off offset:1024
	v_lshlrev_b32_e32 v212, 16, v156
	v_and_b32_e32 v213, 0xffff0000, v156
	v_pk_mul_f32 v[212:213], v[206:207], v[212:213] op_sel_hi:[0,1]
	v_lshlrev_b32_e32 v156, 16, v157
	v_and_b32_e32 v157, 0xffff0000, v157
	v_pk_mul_f32 v[156:157], v[206:207], v[156:157] op_sel_hi:[0,1]
	v_pk_fma_f32 v[212:213], v[20:21], v[212:213], v[52:53]
	v_pk_fma_f32 v[156:157], v[22:23], v[156:157], v[54:55]
	v_cvt_pk_fp8_f32 v215, v212, v213
	v_cvt_pk_fp8_f32 v215, v156, v157 op_sel:[0,0,1]
	global_store_dword v[210:211], v215, off offset:1280
	v_lshlrev_b32_e32 v212, 16, v158
	v_and_b32_e32 v213, 0xffff0000, v158
	v_pk_mul_f32 v[212:213], v[206:207], v[212:213] op_sel_hi:[0,1]
	v_lshlrev_b32_e32 v158, 16, v159
	v_and_b32_e32 v159, 0xffff0000, v159
	v_pk_mul_f32 v[158:159], v[206:207], v[158:159] op_sel_hi:[0,1]
	v_pk_fma_f32 v[212:213], v[24:25], v[212:213], v[56:57]
	v_pk_fma_f32 v[158:159], v[26:27], v[158:159], v[58:59]
	v_cvt_pk_fp8_f32 v214, v212, v213
	v_cvt_pk_fp8_f32 v214, v158, v159 op_sel:[0,0,1]
	global_store_dword v[210:211], v214, off offset:1536
	v_lshlrev_b32_e32 v212, 16, v160
	v_and_b32_e32 v213, 0xffff0000, v160
	v_pk_mul_f32 v[212:213], v[206:207], v[212:213] op_sel_hi:[0,1]
	v_lshlrev_b32_e32 v160, 16, v161
	v_and_b32_e32 v161, 0xffff0000, v161
	v_pk_mul_f32 v[160:161], v[206:207], v[160:161] op_sel_hi:[0,1]
	v_pk_fma_f32 v[212:213], v[28:29], v[212:213], v[198:199]
	v_pk_fma_f32 v[160:161], v[30:31], v[160:161], v[200:201]
	v_cvt_pk_fp8_f32 v215, v212, v213
	v_cvt_pk_fp8_f32 v215, v160, v161 op_sel:[0,0,1]
	global_store_dword v[210:211], v215, off offset:1792
	s_add_u32 s4, s4, 0x800
	v_lshl_add_u64 v[210:211], v[68:69], 0, s[4:5]
	s_waitcnt vmcnt(24)
; __device__ __forceinline__ void phase_router(const Args& a, unsigned char* lds_g, int tid, int lane, int wave) {
;     ...
;     for (int tp = blockIdx.x; tp < NLAT / 32; tp += gridDim.x) {
;     ...
;         for (int r = 0; r < 4; ++r) { const int tl = 4 * kq + r, t = tok0 + tl; const float rstd = RS[slot * 16 + tl];
;             const unsigned long long* xrow = (const unsigned long long*)(X1 + (size_t)t * D) + lane; unsigned* o4 = (unsigned*)((unsigned char*)H2 + (size_t)t * D) + lane;
;             f32x4 yv[8];
; #pragma unroll
;             for (int j = 0; j < 8; ++j) { const int c = 4 * lane + 256 * j;
;                 f32x4 gs, sh; if (shp) { gs = PSH[lane + 64 * j]; sh = PSH[512 + lane + 64 * j]; } else { const f32x4 gg = *(const f32x4*)(g + c), sc = *(const f32x4*)(MOD + b * 12288 + 4 * 2048 + c); gs = gg * (sc + 1.f); sh = *(const f32x4*)(MOD + b * 12288 + 3 * 2048 + c); }
;                 const unsigned long long xw = xrow[64 * j]; const f32x4 xv4 = (f32x4){bflo((unsigned)xw), bfhi((unsigned)xw), bflo((unsigned)(xw >> 32)), bfhi((unsigned)(xw >> 32))};
;                 yv[j] = xv4 * rstd * gs + sh; }
; #pragma unroll
;             for (int j = 0; j < 8; ++j) { int w8 = __builtin_amdgcn_cvt_pk_fp8_f32(yv[j].x, yv[j].y, 0, false); w8 = __builtin_amdgcn_cvt_pk_fp8_f32(yv[j].z, yv[j].w, w8, true); o4[64 * j] = (unsigned)w8; } }
;         __syncthreads();
;     }
	v_lshlrev_b32_e32 v212, 16, v162
	v_and_b32_e32 v213, 0xffff0000, v162
	v_pk_mul_f32 v[212:213], v[208:209], v[212:213] op_sel_hi:[0,1]
	v_lshlrev_b32_e32 v162, 16, v163
	v_and_b32_e32 v163, 0xffff0000, v163
	v_pk_mul_f32 v[162:163], v[208:209], v[162:163] op_sel_hi:[0,1]
	v_pk_fma_f32 v[212:213], v[0:1], v[212:213], v[32:33]
	v_pk_fma_f32 v[162:163], v[2:3], v[162:163], v[34:35]
	v_cvt_pk_fp8_f32 v214, v212, v213
	v_cvt_pk_fp8_f32 v214, v162, v163 op_sel:[0,0,1]
	global_store_dword v[210:211], v214, off
	v_lshlrev_b32_e32 v212, 16, v164
	v_and_b32_e32 v213, 0xffff0000, v164
	v_pk_mul_f32 v[212:213], v[208:209], v[212:213] op_sel_hi:[0,1]
	v_lshlrev_b32_e32 v164, 16, v165
	v_and_b32_e32 v165, 0xffff0000, v165
	v_pk_mul_f32 v[164:165], v[208:209], v[164:165] op_sel_hi:[0,1]
	v_pk_fma_f32 v[212:213], v[4:5], v[212:213], v[36:37]
	v_pk_fma_f32 v[164:165], v[6:7], v[164:165], v[38:39]
	v_cvt_pk_fp8_f32 v215, v212, v213
	v_cvt_pk_fp8_f32 v215, v164, v165 op_sel:[0,0,1]
	global_store_dword v[210:211], v215, off offset:256
	v_lshlrev_b32_e32 v212, 16, v166
	v_and_b32_e32 v213, 0xffff0000, v166
	v_pk_mul_f32 v[212:213], v[208:209], v[212:213] op_sel_hi:[0,1]
	v_lshlrev_b32_e32 v166, 16, v167
	v_and_b32_e32 v167, 0xffff0000, v167
	v_pk_mul_f32 v[166:167], v[208:209], v[166:167] op_sel_hi:[0,1]
	v_pk_fma_f32 v[212:213], v[8:9], v[212:213], v[40:41]
	v_pk_fma_f32 v[166:167], v[10:11], v[166:167], v[42:43]
	v_cvt_pk_fp8_f32 v214, v212, v213
	v_cvt_pk_fp8_f32 v214, v166, v167 op_sel:[0,0,1]
	global_store_dword v[210:211], v214, off offset:512
	v_lshlrev_b32_e32 v212, 16, v168
	v_and_b32_e32 v213, 0xffff0000, v168
	v_pk_mul_f32 v[212:213], v[208:209], v[212:213] op_sel_hi:[0,1]
	v_lshlrev_b32_e32 v168, 16, v169
	v_and_b32_e32 v169, 0xffff0000, v169
	v_pk_mul_f32 v[168:169], v[208:209], v[168:169] op_sel_hi:[0,1]
	v_pk_fma_f32 v[212:213], v[12:13], v[212:213], v[44:45]
	v_pk_fma_f32 v[168:169], v[14:15], v[168:169], v[46:47]
	v_cvt_pk_fp8_f32 v215, v212, v213
	v_cvt_pk_fp8_f32 v215, v168, v169 op_sel:[0,0,1]
	global_store_dword v[210:211], v215, off offset:768
	v_lshlrev_b32_e32 v212, 16, v170
	v_and_b32_e32 v213, 0xffff0000, v170
	v_pk_mul_f32 v[212:213], v[208:209], v[212:213] op_sel_hi:[0,1]
	v_lshlrev_b32_e32 v170, 16, v171
	v_and_b32_e32 v171, 0xffff0000, v171
	v_pk_mul_f32 v[170:171], v[208:209], v[170:171] op_sel_hi:[0,1]
	v_pk_fma_f32 v[212:213], v[16:17], v[212:213], v[48:49]
	v_pk_fma_f32 v[170:171], v[18:19], v[170:171], v[50:51]
	v_cvt_pk_fp8_f32 v214, v212, v213
	v_cvt_pk_fp8_f32 v214, v170, v171 op_sel:[0,0,1]
	global_store_dword v[210:211], v214, off offset:1024
	v_lshlrev_b32_e32 v212, 16, v172
	v_and_b32_e32 v213, 0xffff0000, v172
	v_pk_mul_f32 v[212:213], v[208:209], v[212:213] op_sel_hi:[0,1]
	v_lshlrev_b32_e32 v172, 16, v173
	v_and_b32_e32 v173, 0xffff0000, v173
	v_pk_mul_f32 v[172:173], v[208:209], v[172:173] op_sel_hi:[0,1]
	v_pk_fma_f32 v[212:213], v[20:21], v[212:213], v[52:53]
	v_pk_fma_f32 v[172:173], v[22:23], v[172:173], v[54:55]
	v_cvt_pk_fp8_f32 v215, v212, v213
	v_cvt_pk_fp8_f32 v215, v172, v173 op_sel:[0,0,1]
	global_store_dword v[210:211], v215, off offset:1280
	v_lshlrev_b32_e32 v212, 16, v194
	v_and_b32_e32 v213, 0xffff0000, v194
	v_pk_mul_f32 v[212:213], v[208:209], v[212:213] op_sel_hi:[0,1]
	v_lshlrev_b32_e32 v194, 16, v195
	v_and_b32_e32 v195, 0xffff0000, v195
	v_pk_mul_f32 v[194:195], v[208:209], v[194:195] op_sel_hi:[0,1]
	v_pk_fma_f32 v[212:213], v[24:25], v[212:213], v[56:57]
	v_pk_fma_f32 v[194:195], v[26:27], v[194:195], v[58:59]
	v_cvt_pk_fp8_f32 v214, v212, v213
	v_cvt_pk_fp8_f32 v214, v194, v195 op_sel:[0,0,1]
	global_store_dword v[210:211], v214, off offset:1536
	v_lshlrev_b32_e32 v212, 16, v196
	v_and_b32_e32 v213, 0xffff0000, v196
	v_pk_mul_f32 v[212:213], v[208:209], v[212:213] op_sel_hi:[0,1]
	v_lshlrev_b32_e32 v196, 16, v197
	v_and_b32_e32 v197, 0xffff0000, v197
	v_pk_mul_f32 v[196:197], v[208:209], v[196:197] op_sel_hi:[0,1]
	v_pk_fma_f32 v[212:213], v[28:29], v[212:213], v[198:199]
	v_pk_fma_f32 v[196:197], v[30:31], v[196:197], v[200:201]
	v_cvt_pk_fp8_f32 v215, v212, v213
	v_cvt_pk_fp8_f32 v215, v196, v197 op_sel:[0,0,1]
	global_store_dword v[210:211], v215, off offset:1792
	s_add_i32 s55, s55, s82
	v_add_u32_e32 v106, s44, v106
	s_cmpk_lt_i32 s55, 0x100
	s_barrier
	s_cbranch_scc0 .LBB0_1113
	s_branch .LBB0_975
.Lh2_old:
	s_add_u32 s30, s4, 0x8000
	ds_read_b32 v60, v0 offset:50176
	s_addc_u32 s31, s5, 0
	s_add_u32 s6, s4, 0x6000
	s_addc_u32 s7, s5, 0
	v_lshlrev_b64 v[146:147], 2, v[62:63]
	s_mov_b64 s[4:5], -1
	s_and_b64 vcc, exec, s[18:19]
	v_lshl_add_u64 v[126:127], s[30:31], 0, v[146:147]
	v_lshl_add_u64 v[116:117], s[6:7], 0, v[146:147]
	s_cbranch_vccz .LBB0_987
	global_load_dwordx4 v[0:3], v[126:127], off
	global_load_dwordx4 v[6:9], v[70:71], off
	v_lshl_add_u64 v[4:5], s[6:7], 0, v[146:147]
	s_mov_b64 s[4:5], 0
	s_waitcnt vmcnt(1)
	v_pk_add_f32 v[2:3], v[2:3], 1.0 op_sel_hi:[1,0]
	v_pk_add_f32 v[0:1], v[0:1], 1.0 op_sel_hi:[1,0]
	s_waitcnt vmcnt(0)
	v_pk_mul_f32 v[2:3], v[8:9], v[2:3]
	v_pk_mul_f32 v[0:1], v[6:7], v[0:1]
